# speedup vs baseline: 1.0039x; 1.0039x over previous
.Lprep_noflag:
	v_lshl_add_u64 v[2:3], s[8:9], 0, v[0:1]
	s_mov_b64 s[12:13], 0x1000000
	global_load_dwordx4 v[20:23], v[2:3], off offset:16 sc1 nt
	global_load_dwordx4 v[28:31], v[2:3], off sc1 nt
	v_lshl_add_u64 v[4:5], v[2:3], 0, s[12:13]
	v_add_co_u32_e32 v2, vcc, 0x1000000, v2
	v_lshl_add_u64 v[0:1], s[10:11], 0, v[0:1]
	s_nop 0
	v_addc_co_u32_e32 v3, vcc, 0, v3, vcc
	global_load_dwordx4 v[24:27], v[2:3], off sc1 nt
	global_load_dwordx4 v[16:19], v[4:5], off offset:16 sc1 nt
	s_nop 0
	global_load_dwordx4 v[4:7], v[0:1], off offset:16 sc1 nt
	global_load_dwordx4 v[8:11], v[0:1], off sc1 nt
	s_cmpk_lt_u32 s14, 0x500
	s_cselect_b64 s[8:9], -1, 0
	s_cmpk_gt_u32 s14, 0x4ff
	v_mov_b32_e32 v1, v35
	v_mov_b32_e32 v2, v35
	v_mov_b32_e32 v3, v35
	v_mov_b32_e32 v12, v35
	v_mov_b32_e32 v13, v35
	v_mov_b32_e32 v14, v35
	v_mov_b32_e32 v15, v35
	s_cbranch_scc1 .LBB0_3
	v_lshl_add_u64 v[0:1], v[32:33], 2, s[10:11]
	v_add_co_u32_e32 v36, vcc, 0x1000000, v0
	v_lshl_add_u64 v[34:35], v[0:1], 0, s[12:13]
	s_nop 0
	v_addc_co_u32_e32 v37, vcc, 0, v1, vcc
	global_load_dwordx4 v[0:3], v[36:37], off sc1 nt
	global_load_dwordx4 v[12:15], v[34:35], off offset:16 sc1 nt
	s_waitcnt vmcnt(1)
	v_mov_b32_e32 v35, v0
